# hybrid K1 with ring 32 (32KiB chunks, 7 private + queues), 8KiB bursts
# speedup vs baseline: 1.0366x; 1.0366x over previous
.Lk1_scan:
	s_load_dwordx2 s[4:5], s[0:1], 0x0
	s_load_dwordx4 s[8:11], s[0:1], 0x20
	s_load_dwordx2 s[12:13], s[0:1], 0x30
	v_and_b32_e32 v6, 63, v0
	v_readfirstlane_b32 s3, v0
	v_lshlrev_b32_e32 v1, 4, v6
	v_lshlrev_b32_e32 v2, 2, v6
	v_or_b32_e32 v3, 1, v2
	v_or_b32_e32 v4, 2, v2
	v_or_b32_e32 v5, 3, v2
	s_lshr_b32 s3, s3, 6
	s_sub_u32 s16, s2, 0x60
	s_lshl_b32 s16, s16, 2
	s_add_u32 s16, s16, s3
	s_mul_i32 s17, s16, 0x48000
	s_lshr_b32 s18, s17, 2
	s_lshl_b32 s24, s3, 13
	s_mov_b32 s25, s24
	s_mov_b32 s28, s24
	s_mov_b32 s36, 0
	v_mov_b32_e32 v21, 1
	s_mov_b32 s27, 0
	s_mov_b32 s29, 0x55555556
	s_mov_b32 s31, 0xc0000
	s_waitcnt lgkmcnt(0)
	s_and_b32 s50, s16, 15
	s_mul_i32 s52, s50, 256
	s_add_u32 s52, s52, 14336
	s_lshl_b32 s53, s50, 6
	s_add_u32 s53, s53, 0xe000
	s_add_u32 s54, s10, s53
	s_addc_u32 s55, s11, 0
	s_mul_i32 s59, s16, 7
	s_mul_i32 s57, s59, 0x8000
	s_lshr_b32 s18, s57, 2
	s_add_u32 s6, s4, s57
	s_addc_u32 s7, s5, 0
	v_mov_b32_e32 v27, 0
	global_load_dwordx4 v[28:31], v1, s[6:7] nt
	s_add_u32 s6, s6, 0x400
	s_addc_u32 s7, s7, 0
	global_load_dwordx4 v[32:35], v1, s[6:7] nt
	s_add_u32 s6, s6, 0x400
	s_addc_u32 s7, s7, 0
	global_load_dwordx4 v[36:39], v1, s[6:7] nt
	s_add_u32 s6, s6, 0x400
	s_addc_u32 s7, s7, 0
	global_load_dwordx4 v[40:43], v1, s[6:7] nt
	s_add_u32 s6, s6, 0x400
	s_addc_u32 s7, s7, 0
	global_load_dwordx4 v[44:47], v1, s[6:7] nt
	s_add_u32 s6, s6, 0x400
	s_addc_u32 s7, s7, 0
	global_load_dwordx4 v[48:51], v1, s[6:7] nt
	s_add_u32 s6, s6, 0x400
	s_addc_u32 s7, s7, 0
	global_load_dwordx4 v[52:55], v1, s[6:7] nt
	s_add_u32 s6, s6, 0x400
	s_addc_u32 s7, s7, 0
	global_load_dwordx4 v[56:59], v1, s[6:7] nt
	s_add_u32 s6, s6, 0x400
	s_addc_u32 s7, s7, 0
	global_load_dwordx4 v[60:63], v1, s[6:7] nt
	s_add_u32 s6, s6, 0x400
	s_addc_u32 s7, s7, 0
	global_load_dwordx4 v[64:67], v1, s[6:7] nt
	s_add_u32 s6, s6, 0x400
	s_addc_u32 s7, s7, 0
	global_load_dwordx4 v[68:71], v1, s[6:7] nt
	s_add_u32 s6, s6, 0x400
	s_addc_u32 s7, s7, 0
	global_load_dwordx4 v[72:75], v1, s[6:7] nt
	s_add_u32 s6, s6, 0x400
	s_addc_u32 s7, s7, 0
	global_load_dwordx4 v[76:79], v1, s[6:7] nt
	s_add_u32 s6, s6, 0x400
	s_addc_u32 s7, s7, 0
	global_load_dwordx4 v[80:83], v1, s[6:7] nt
	s_add_u32 s6, s6, 0x400
	s_addc_u32 s7, s7, 0
	global_load_dwordx4 v[84:87], v1, s[6:7] nt
	s_add_u32 s6, s6, 0x400
	s_addc_u32 s7, s7, 0
	global_load_dwordx4 v[88:91], v1, s[6:7] nt
	s_add_u32 s6, s6, 0x400
	s_addc_u32 s7, s7, 0
	global_load_dwordx4 v[92:95], v1, s[6:7] nt
	s_add_u32 s6, s6, 0x400
	s_addc_u32 s7, s7, 0
	global_load_dwordx4 v[96:99], v1, s[6:7] nt
	s_add_u32 s6, s6, 0x400
	s_addc_u32 s7, s7, 0
	global_load_dwordx4 v[100:103], v1, s[6:7] nt
	s_add_u32 s6, s6, 0x400
	s_addc_u32 s7, s7, 0
	global_load_dwordx4 v[104:107], v1, s[6:7] nt
	s_add_u32 s6, s6, 0x400
	s_addc_u32 s7, s7, 0
	global_load_dwordx4 v[108:111], v1, s[6:7] nt
	s_add_u32 s6, s6, 0x400
	s_addc_u32 s7, s7, 0
	global_load_dwordx4 v[112:115], v1, s[6:7] nt
	s_add_u32 s6, s6, 0x400
	s_addc_u32 s7, s7, 0
	global_load_dwordx4 v[116:119], v1, s[6:7] nt
	s_add_u32 s6, s6, 0x400
	s_addc_u32 s7, s7, 0
	global_load_dwordx4 v[120:123], v1, s[6:7] nt
	s_add_u32 s6, s6, 0x400
	s_addc_u32 s7, s7, 0
	global_load_dwordx4 v[124:127], v1, s[6:7] nt
	s_add_u32 s6, s6, 0x400
	s_addc_u32 s7, s7, 0
	global_load_dwordx4 v[128:131], v1, s[6:7] nt
	s_add_u32 s6, s6, 0x400
	s_addc_u32 s7, s7, 0
	global_load_dwordx4 v[132:135], v1, s[6:7] nt
	s_add_u32 s6, s6, 0x400
	s_addc_u32 s7, s7, 0
	global_load_dwordx4 v[136:139], v1, s[6:7] nt
	s_add_u32 s6, s6, 0x400
	s_addc_u32 s7, s7, 0
	global_load_dwordx4 v[140:143], v1, s[6:7] nt
	s_add_u32 s6, s6, 0x400
	s_addc_u32 s7, s7, 0
	global_load_dwordx4 v[144:147], v1, s[6:7] nt
	s_add_u32 s6, s6, 0x400
	s_addc_u32 s7, s7, 0
	global_load_dwordx4 v[148:151], v1, s[6:7] nt
	s_add_u32 s6, s6, 0x400
	s_addc_u32 s7, s7, 0
	global_load_dwordx4 v[152:155], v1, s[6:7] nt
	s_add_u32 s6, s6, 0x400
	s_addc_u32 s7, s7, 0
	s_mov_b32 s26, 9
	s_add_u32 s57, s59, 1
	s_mul_i32 s57, s57, 0x8000
	s_lshr_b32 s58, s57, 2
	s_add_u32 s6, s4, s57
	s_addc_u32 s7, s5, 0
	s_mov_b32 s26, 0

.Lk1_contm_7:
	global_load_dwordx4 v[28:31], v1, s[6:7] nt
	s_add_u32 s6, s6, 0x400
	s_addc_u32 s7, s7, 0
	global_load_dwordx4 v[32:35], v1, s[6:7] nt
	s_add_u32 s6, s6, 0x400
	s_addc_u32 s7, s7, 0
	global_load_dwordx4 v[36:39], v1, s[6:7] nt
	s_add_u32 s6, s6, 0x400
	s_addc_u32 s7, s7, 0
	global_load_dwordx4 v[40:43], v1, s[6:7] nt
	s_add_u32 s6, s6, 0x400
	s_addc_u32 s7, s7, 0
	global_load_dwordx4 v[44:47], v1, s[6:7] nt
	s_add_u32 s6, s6, 0x400
	s_addc_u32 s7, s7, 0
	global_load_dwordx4 v[48:51], v1, s[6:7] nt
	s_add_u32 s6, s6, 0x400
	s_addc_u32 s7, s7, 0
	global_load_dwordx4 v[52:55], v1, s[6:7] nt
	s_add_u32 s6, s6, 0x400
	s_addc_u32 s7, s7, 0
	global_load_dwordx4 v[56:59], v1, s[6:7] nt
	s_add_u32 s6, s6, 0x400
	s_addc_u32 s7, s7, 0
	s_waitcnt vmcnt(31)
	v_or3_b32 v12, v60, v61, v62
	v_or_b32_e32 v12, v12, v63
	v_cmp_ne_u32_e32 vcc, 0, v12
	s_cbranch_vccnz .Lk1_hitm_8
.Lk1_contm_8:
	s_waitcnt vmcnt(30)
	v_or3_b32 v12, v64, v65, v66
	v_or_b32_e32 v12, v12, v67
	v_cmp_ne_u32_e32 vcc, 0, v12
	s_cbranch_vccnz .Lk1_hitm_9
.Lk1_contm_9:
	s_waitcnt vmcnt(29)
	v_or3_b32 v12, v68, v69, v70
	v_or_b32_e32 v12, v12, v71
	v_cmp_ne_u32_e32 vcc, 0, v12
	s_cbranch_vccnz .Lk1_hitm_10
.Lk1_contm_10:
	s_waitcnt vmcnt(28)
	v_or3_b32 v12, v72, v73, v74
	v_or_b32_e32 v12, v12, v75
	v_cmp_ne_u32_e32 vcc, 0, v12
	s_cbranch_vccnz .Lk1_hitm_11
.Lk1_contm_11:
	s_waitcnt vmcnt(27)
	v_or3_b32 v12, v76, v77, v78
	v_or_b32_e32 v12, v12, v79
	v_cmp_ne_u32_e32 vcc, 0, v12
	s_cbranch_vccnz .Lk1_hitm_12
.Lk1_contm_12:
	s_waitcnt vmcnt(26)
	v_or3_b32 v12, v80, v81, v82
	v_or_b32_e32 v12, v12, v83
	v_cmp_ne_u32_e32 vcc, 0, v12
	s_cbranch_vccnz .Lk1_hitm_13
.Lk1_contm_13:
	s_waitcnt vmcnt(25)
	v_or3_b32 v12, v84, v85, v86
	v_or_b32_e32 v12, v12, v87
	v_cmp_ne_u32_e32 vcc, 0, v12
	s_cbranch_vccnz .Lk1_hitm_14
.Lk1_contm_14:
	s_waitcnt vmcnt(24)
	v_or3_b32 v12, v88, v89, v90
	v_or_b32_e32 v12, v12, v91
	v_cmp_ne_u32_e32 vcc, 0, v12
	s_cbranch_vccnz .Lk1_hitm_15
.Lk1_contm_15:
	global_load_dwordx4 v[60:63], v1, s[6:7] nt
	s_add_u32 s6, s6, 0x400
	s_addc_u32 s7, s7, 0
	global_load_dwordx4 v[64:67], v1, s[6:7] nt
	s_add_u32 s6, s6, 0x400
	s_addc_u32 s7, s7, 0
	global_load_dwordx4 v[68:71], v1, s[6:7] nt
	s_add_u32 s6, s6, 0x400
	s_addc_u32 s7, s7, 0
	global_load_dwordx4 v[72:75], v1, s[6:7] nt
	s_add_u32 s6, s6, 0x400
	s_addc_u32 s7, s7, 0
	global_load_dwordx4 v[76:79], v1, s[6:7] nt
	s_add_u32 s6, s6, 0x400
	s_addc_u32 s7, s7, 0
	global_load_dwordx4 v[80:83], v1, s[6:7] nt
	s_add_u32 s6, s6, 0x400
	s_addc_u32 s7, s7, 0
	global_load_dwordx4 v[84:87], v1, s[6:7] nt
	s_add_u32 s6, s6, 0x400
	s_addc_u32 s7, s7, 0
	global_load_dwordx4 v[88:91], v1, s[6:7] nt
	s_add_u32 s6, s6, 0x400
	s_addc_u32 s7, s7, 0
	s_waitcnt vmcnt(31)
	v_or3_b32 v12, v92, v93, v94
	v_or_b32_e32 v12, v12, v95
	v_cmp_ne_u32_e32 vcc, 0, v12
	s_cbranch_vccnz .Lk1_hitm_16
.Lk1_contm_16:
	s_waitcnt vmcnt(30)
	v_or3_b32 v12, v96, v97, v98
	v_or_b32_e32 v12, v12, v99
	v_cmp_ne_u32_e32 vcc, 0, v12
	s_cbranch_vccnz .Lk1_hitm_17
.Lk1_contm_17:
	s_waitcnt vmcnt(29)
	v_or3_b32 v12, v100, v101, v102
	v_or_b32_e32 v12, v12, v103
	v_cmp_ne_u32_e32 vcc, 0, v12
	s_cbranch_vccnz .Lk1_hitm_18
.Lk1_contm_18:
	s_waitcnt vmcnt(28)
	v_or3_b32 v12, v104, v105, v106
	v_or_b32_e32 v12, v12, v107
	v_cmp_ne_u32_e32 vcc, 0, v12
	s_cbranch_vccnz .Lk1_hitm_19
.Lk1_contm_19:
	s_waitcnt vmcnt(27)
	v_or3_b32 v12, v108, v109, v110
	v_or_b32_e32 v12, v12, v111
	v_cmp_ne_u32_e32 vcc, 0, v12
	s_cbranch_vccnz .Lk1_hitm_20
.Lk1_contm_20:
	s_waitcnt vmcnt(26)
	v_or3_b32 v12, v112, v113, v114
	v_or_b32_e32 v12, v12, v115
	v_cmp_ne_u32_e32 vcc, 0, v12
	s_cbranch_vccnz .Lk1_hitm_21
.Lk1_contm_21:
	s_waitcnt vmcnt(25)
	v_or3_b32 v12, v116, v117, v118
	v_or_b32_e32 v12, v12, v119
	v_cmp_ne_u32_e32 vcc, 0, v12
	s_cbranch_vccnz .Lk1_hitm_22
.Lk1_contm_22:
	s_waitcnt vmcnt(24)
	v_or3_b32 v12, v120, v121, v122
	v_or_b32_e32 v12, v12, v123
	v_cmp_ne_u32_e32 vcc, 0, v12
	s_cbranch_vccnz .Lk1_hitm_23
.Lk1_contm_23:
	global_load_dwordx4 v[92:95], v1, s[6:7] nt
	s_add_u32 s6, s6, 0x400
	s_addc_u32 s7, s7, 0
	global_load_dwordx4 v[96:99], v1, s[6:7] nt
	s_add_u32 s6, s6, 0x400
	s_addc_u32 s7, s7, 0
	global_load_dwordx4 v[100:103], v1, s[6:7] nt
	s_add_u32 s6, s6, 0x400
	s_addc_u32 s7, s7, 0
	global_load_dwordx4 v[104:107], v1, s[6:7] nt
	s_add_u32 s6, s6, 0x400
	s_addc_u32 s7, s7, 0
	global_load_dwordx4 v[108:111], v1, s[6:7] nt
	s_add_u32 s6, s6, 0x400
	s_addc_u32 s7, s7, 0
	global_load_dwordx4 v[112:115], v1, s[6:7] nt
	s_add_u32 s6, s6, 0x400
	s_addc_u32 s7, s7, 0
	global_load_dwordx4 v[116:119], v1, s[6:7] nt
	s_add_u32 s6, s6, 0x400
	s_addc_u32 s7, s7, 0
	global_load_dwordx4 v[120:123], v1, s[6:7] nt
	s_add_u32 s6, s6, 0x400
	s_addc_u32 s7, s7, 0
	s_waitcnt vmcnt(31)
	v_or3_b32 v12, v124, v125, v126
	v_or_b32_e32 v12, v12, v127
	v_cmp_ne_u32_e32 vcc, 0, v12
	s_cbranch_vccnz .Lk1_hitm_24
.Lk1_contm_24:
	s_waitcnt vmcnt(30)
	v_or3_b32 v12, v128, v129, v130
	v_or_b32_e32 v12, v12, v131
	v_cmp_ne_u32_e32 vcc, 0, v12
	s_cbranch_vccnz .Lk1_hitm_25
.Lk1_contm_25:
	s_waitcnt vmcnt(29)
	v_or3_b32 v12, v132, v133, v134
	v_or_b32_e32 v12, v12, v135
	v_cmp_ne_u32_e32 vcc, 0, v12
	s_cbranch_vccnz .Lk1_hitm_26
.Lk1_contm_26:
	s_waitcnt vmcnt(28)
	v_or3_b32 v12, v136, v137, v138
	v_or_b32_e32 v12, v12, v139
	v_cmp_ne_u32_e32 vcc, 0, v12
	s_cbranch_vccnz .Lk1_hitm_27
.Lk1_contm_27:
	s_waitcnt vmcnt(27)
	v_or3_b32 v12, v140, v141, v142
	v_or_b32_e32 v12, v12, v143
	v_cmp_ne_u32_e32 vcc, 0, v12
	s_cbranch_vccnz .Lk1_hitm_28
.Lk1_contm_28:
	s_waitcnt vmcnt(26)
	v_or3_b32 v12, v144, v145, v146
	v_or_b32_e32 v12, v12, v147
	v_cmp_ne_u32_e32 vcc, 0, v12
	s_cbranch_vccnz .Lk1_hitm_29
.Lk1_contm_29:
	s_waitcnt vmcnt(25)
	v_or3_b32 v12, v148, v149, v150
	v_or_b32_e32 v12, v12, v151
	v_cmp_ne_u32_e32 vcc, 0, v12
	s_cbranch_vccnz .Lk1_hitm_30
.Lk1_contm_30:
	s_waitcnt vmcnt(24)
	v_or3_b32 v12, v152, v153, v154
	v_or_b32_e32 v12, v12, v155
	v_cmp_ne_u32_e32 vcc, 0, v12
	s_cbranch_vccnz .Lk1_hitm_31
.Lk1_contm_31:
	global_load_dwordx4 v[124:127], v1, s[6:7] nt
	s_add_u32 s6, s6, 0x400
	s_addc_u32 s7, s7, 0
	global_load_dwordx4 v[128:131], v1, s[6:7] nt
	s_add_u32 s6, s6, 0x400
	s_addc_u32 s7, s7, 0
	global_load_dwordx4 v[132:135], v1, s[6:7] nt
	s_add_u32 s6, s6, 0x400
	s_addc_u32 s7, s7, 0
	global_load_dwordx4 v[136:139], v1, s[6:7] nt
	s_add_u32 s6, s6, 0x400
	s_addc_u32 s7, s7, 0
	global_load_dwordx4 v[140:143], v1, s[6:7] nt
	s_add_u32 s6, s6, 0x400
	s_addc_u32 s7, s7, 0
	global_load_dwordx4 v[144:147], v1, s[6:7] nt
	s_add_u32 s6, s6, 0x400
	s_addc_u32 s7, s7, 0
	global_load_dwordx4 v[148:151], v1, s[6:7] nt
	s_add_u32 s6, s6, 0x400
	s_addc_u32 s7, s7, 0
	global_load_dwordx4 v[152:155], v1, s[6:7] nt
	s_add_u32 s6, s6, 0x400
	s_addc_u32 s7, s7, 0
	s_mov_b32 s18, s58
	s_add_u32 s60, s26, 2
	s_cmp_lt_u32 s60, 7
	s_cbranch_scc0 .Lk1_dynid
	s_add_u32 s57, s59, s60
	s_branch .Lk1_haveid
.Lk1_dynid:
	v_readfirstlane_b32 s56, v26
	s_nop 0
	s_cmp_lt_u32 s56, 256
	s_cbranch_scc0 .Lk1_lastchunk
	s_add_u32 s57, s52, s56
.Lk1_haveid:
	s_mul_i32 s57, s57, 0x8000
	s_lshr_b32 s58, s57, 2
	s_add_u32 s6, s4, s57
	s_addc_u32 s7, s5, 0
	s_add_u32 s60, s26, 3
	s_cmp_lt_u32 s60, 7
	s_cbranch_scc1 .Lk1_noreq
	s_mov_b64 exec, 1
	global_atomic_add v26, v27, v21, s[54:55] sc0
	s_mov_b64 exec, -1

amdhsa.kernels:
  - .agpr_count:     0
    .args:
      - .actual_access:  read_only
        .address_space:  global
        .offset:         0
        .size:           8
        .value_kind:     global_buffer
      - .actual_access:  read_only
        .address_space:  global
        .offset:         8
        .size:           8
        .value_kind:     global_buffer
      - .actual_access:  read_only
        .address_space:  global
        .offset:         16
        .size:           8
        .value_kind:     global_buffer
      - .actual_access:  write_only
        .address_space:  global
        .offset:         24
        .size:           8
        .value_kind:     global_buffer
      - .address_space:  global
        .offset:         32
        .size:           8
        .value_kind:     global_buffer
      - .address_space:  global
        .offset:         40
        .size:           8
        .value_kind:     global_buffer
      - .actual_access:  write_only
        .address_space:  global
        .offset:         48
        .size:           8
        .value_kind:     global_buffer
      - .actual_access:  write_only
        .address_space:  global
        .offset:         56
        .size:           8
        .value_kind:     global_buffer
    .group_segment_fixed_size: 37392
    .kernarg_segment_align: 8
    .kernarg_segment_size: 64
    .language:       OpenCL C
    .language_version:
      - 2
      - 0
    .max_flat_workgroup_size: 256
    .name:           _Z9k1_kernelPKfS0_S0_PDF16_PiPfP15HIP_vector_typeIiLj2EES6_
    .private_segment_fixed_size: 0
    .sgpr_count:     32
    .sgpr_spill_count: 0
    .symbol:         _Z9k1_kernelPKfS0_S0_PDF16_PiPfP15HIP_vector_typeIiLj2EES6_.kd
    .uniform_work_group_size: 1
    .uses_dynamic_stack: false
    .vgpr_count:     156
    .vgpr_spill_count: 0
    .wavefront_size: 64
  - .agpr_count:     0
    .args:
      - .actual_access:  read_only
        .address_space:  global
        .offset:         0
        .size:           8
        .value_kind:     global_buffer
      - .actual_access:  read_only
        .address_space:  global
        .offset:         8
        .size:           8
        .value_kind:     global_buffer
      - .actual_access:  read_only
        .address_space:  global
        .offset:         16
        .size:           8
        .value_kind:     global_buffer
      - .actual_access:  read_only
        .address_space:  global
        .offset:         24
        .size:           8
        .value_kind:     global_buffer
      - .actual_access:  read_only
        .address_space:  global
        .offset:         32
        .size:           8
        .value_kind:     global_buffer
      - .actual_access:  read_only
        .address_space:  global
        .offset:         40
        .size:           8
        .value_kind:     global_buffer
      - .actual_access:  read_only
        .address_space:  global
        .offset:         48
        .size:           8
        .value_kind:     global_buffer
      - .actual_access:  read_only
        .address_space:  global
        .offset:         56
        .size:           8
        .value_kind:     global_buffer
      - .actual_access:  read_only
        .address_space:  global
        .offset:         64
        .size:           8
        .value_kind:     global_buffer
      - .actual_access:  write_only
        .address_space:  global
        .offset:         72
        .size:           8
        .value_kind:     global_buffer
      - .address_space:  global
        .offset:         80
        .size:           8
        .value_kind:     global_buffer
    .group_segment_fixed_size: 44224
    .kernarg_segment_align: 8
    .kernarg_segment_size: 88
    .language:       OpenCL C
    .language_version:
      - 2
      - 0
    .max_flat_workgroup_size: 512
    .name:           _Z11agg2_kernelPKiPKfPK15HIP_vector_typeIiLj2EEPKDF16_S2_S2_S2_S2_S2_PfS9_
    .private_segment_fixed_size: 0
    .sgpr_count:     41
    .sgpr_spill_count: 0
    .symbol:         _Z11agg2_kernelPKiPKfPK15HIP_vector_typeIiLj2EEPKDF16_S2_S2_S2_S2_S2_PfS9_.kd
    .uniform_work_group_size: 1
    .uses_dynamic_stack: false
    .vgpr_count:     80
    .vgpr_spill_count: 0
    .wavefront_size: 64
  - .agpr_count:     0
    .args:
      - .actual_access:  read_only
        .address_space:  global
        .offset:         0
        .size:           8
        .value_kind:     global_buffer
      - .actual_access:  read_only
        .address_space:  global
        .offset:         8
        .size:           8
        .value_kind:     global_buffer
      - .actual_access:  read_only
        .address_space:  global
        .offset:         16
        .size:           8
        .value_kind:     global_buffer
      - .actual_access:  read_only
        .address_space:  global
        .offset:         24
        .size:           8
        .value_kind:     global_buffer
      - .actual_access:  write_only
        .address_space:  global
        .offset:         32
        .size:           8
        .value_kind:     global_buffer
      - .offset:         40
        .size:           4
        .value_kind:     hidden_block_count_x
      - .offset:         44
        .size:           4
        .value_kind:     hidden_block_count_y
      - .offset:         48
        .size:           4
        .value_kind:     hidden_block_count_z
      - .offset:         52
        .size:           2
        .value_kind:     hidden_group_size_x
      - .offset:         54
        .size:           2
        .value_kind:     hidden_group_size_y
      - .offset:         56
        .size:           2
        .value_kind:     hidden_group_size_z
      - .offset:         58
        .size:           2
        .value_kind:     hidden_remainder_x
      - .offset:         60
        .size:           2
        .value_kind:     hidden_remainder_y
      - .offset:         62
        .size:           2
        .value_kind:     hidden_remainder_z
      - .offset:         80
        .size:           8
        .value_kind:     hidden_global_offset_x
      - .offset:         88
        .size:           8
        .value_kind:     hidden_global_offset_y
      - .offset:         96
        .size:           8
        .value_kind:     hidden_global_offset_z
      - .offset:         104
        .size:           2
        .value_kind:     hidden_grid_dims
    .group_segment_fixed_size: 512
    .kernarg_segment_align: 8
    .kernarg_segment_size: 296
    .language:       OpenCL C
    .language_version:
      - 2
      - 0
    .max_flat_workgroup_size: 256
    .name:           _Z12final_kernelPKfS0_S0_S0_Pf
    .private_segment_fixed_size: 0
    .sgpr_count:     22
    .sgpr_spill_count: 0
    .symbol:         _Z12final_kernelPKfS0_S0_S0_Pf.kd
    .uniform_work_group_size: 1
    .uses_dynamic_stack: false
    .vgpr_count:     49
    .vgpr_spill_count: 0
    .wavefront_size: 64
  - .agpr_count:     0
    .args:
      - .actual_access:  read_only
        .address_space:  global
        .offset:         0
        .size:           8
        .value_kind:     global_buffer
      - .actual_access:  read_only
        .address_space:  global
        .offset:         8
        .size:           8
        .value_kind:     global_buffer
      - .address_space:  global
        .offset:         16
        .size:           8
        .value_kind:     global_buffer
      - .address_space:  global
        .offset:         24
        .size:           8
        .value_kind:     global_buffer
      - .actual_access:  read_only
        .address_space:  global
        .offset:         32
        .size:           8
        .value_kind:     global_buffer
      - .actual_access:  read_only
        .address_space:  global
        .offset:         40
        .size:           8
        .value_kind:     global_buffer
      - .actual_access:  write_only
        .address_space:  global
        .offset:         48
        .size:           8
        .value_kind:     global_buffer
      - .address_space:  global
        .offset:         56
        .size:           8
        .value_kind:     global_buffer
    .group_segment_fixed_size: 8192
    .kernarg_segment_align: 8
    .kernarg_segment_size: 64
    .language:       OpenCL C
    .language_version:
      - 2
      - 0
    .max_flat_workgroup_size: 512
    .name:           _Z10agg_kernelILi128ELb1EEvPKiPKfP15HIP_vector_typeIiLj2EES6_PKDF16_S3_PDF16_Pf
    .private_segment_fixed_size: 0
    .sgpr_count:     42
    .sgpr_spill_count: 0
    .symbol:         _Z10agg_kernelILi128ELb1EEvPKiPKfP15HIP_vector_typeIiLj2EES6_PKDF16_S3_PDF16_Pf.kd
    .uniform_work_group_size: 1
    .uses_dynamic_stack: false
    .vgpr_count:     80
    .vgpr_spill_count: 0
    .wavefront_size: 64
